# weight-copy partition: 2048 more MoE items per layer (vs baseline) moved from the prologue to the forgetting-attention workgroups at the end of the attention phase
# speedup vs baseline: 1.0073x; 1.0052x over previous
.LBB0_16:
	s_mul_i32 s0, s33, 0x4200
	s_add_i32 s0, s0, 0
	v_writelane_b32 v247, s22, 11
	s_cmpk_lg_i32 s3, 0x100
	v_writelane_b32 v247, s0, 13
	s_cselect_b64 s[0:1], -1, 0
	s_cmpk_eq_i32 s3, 0x100
	v_writelane_b32 v247, s0, 14
	s_cselect_b64 s[36:37], -1, 0
	s_mov_b32 s5, 0
	v_writelane_b32 v247, s1, 15
	s_and_b64 s[0:1], s[36:37], exec
	s_cselect_b32 s0, 0x1c00, 0
	s_sub_i32 s1, 0x6000, s0
	s_lshl_b32 s14, s1, 1
	s_addk_i32 s14, 0x1700
	s_cmp_ge_i32 s56, s14
	s_movk_i32 s15, 0x6000
	s_waitcnt lgkmcnt(0)
	s_barrier
	s_cbranch_scc1 .LBB0_27
	v_lshlrev_b32_e32 v0, 1, v12
	v_ashrrev_i32_e32 v4, 5, v12
	v_and_b32_e32 v0, 62, v0
	s_movk_i32 s4, 0x104
	v_lshlrev_b32_e32 v2, 2, v0
	v_mul_lo_u32 v3, v4, s4
	v_readlane_b32 s4, v247, 13
	v_cvt_f32_u32_e32 v9, s1
	v_lshlrev_b32_e32 v6, 2, v13
	v_add3_u32 v5, s4, v2, v3
	v_lshlrev_b32_e32 v2, 3, v12
	v_and_b32_e32 v2, 56, v2
	v_mul_u32_u24_e32 v3, 0x104, v2
	v_add3_u32 v6, s4, v3, v6
	v_rcp_iflag_f32_e32 v3, v9
	s_sub_i32 s4, 0, s1
	v_mov_b32_e32 v1, 0
	v_add_u32_e32 v7, 8, v13
	v_mul_f32_e32 v3, 0x4f7ffffe, v3
	v_cvt_u32_f32_e32 v3, v3
	v_add_u32_e32 v8, 16, v13
	v_add_u32_e32 v9, 24, v13
	v_add_u32_e32 v10, 32, v13
	v_readfirstlane_b32 s10, v3
	s_mul_i32 s4, s4, s10
	s_mul_hi_u32 s4, s10, s4
	s_add_i32 s16, s10, s4
	s_lshl_b32 s4, s0, 1
	s_add_i32 s4, s33, s4
	v_readlane_b32 s10, v247, 8
	s_add_i32 s4, s4, s10
	v_add_u32_e32 v11, 40, v13
	v_add_u32_e32 v14, 48, v13
	v_add_u32_e32 v15, 56, v13
	s_sub_i32 s17, 0xd6ff, s4
	s_movk_i32 s18, 0x4000
	s_mov_b32 s19, 0x8000
	s_mov_b32 s20, 0xc000
	s_mov_b32 s21, 0x10000
	s_mov_b32 s22, 0x14000
	s_mov_b32 s23, 0x18000
	s_mov_b32 s24, 0x1c000
	s_mov_b32 s25, 0x20000
	s_mov_b32 s26, 0x24000
	s_mov_b32 s27, 0x28000
	s_mov_b32 s28, 0x2c000
	s_mov_b32 s29, 0x30000
	s_mov_b32 s30, 0x34000
	s_mov_b32 s31, 0x38000
	s_mov_b32 s34, 0x3c000
	s_mov_b32 s35, 0x40000
	s_mov_b32 s38, 0x44000
	s_mov_b32 s39, 0x48000
	s_mov_b32 s40, 0x4c000
	s_mov_b32 s41, 0x50000
	s_mov_b32 s42, 0x54000
	s_mov_b32 s43, 0x58000
	s_mov_b32 s44, 0x5c000
	s_mov_b32 s45, 0x60000
	s_mov_b32 s46, 0x64000
	s_mov_b32 s47, 0x68000
	s_mov_b32 s48, 0x6c000
	s_mov_b32 s49, 0x70000
	s_mov_b32 s50, 0x74000
	s_mov_b32 s51, 0x78000
	s_mov_b32 s52, 0x7c000
	v_add_u32_e32 v16, 0x410, v5
	v_add_u32_e32 v17, 0x618, v5
	v_add_u32_e32 v18, 0x820, v5
	v_add_u32_e32 v19, 0xa28, v5
	v_add_u32_e32 v20, 0xc30, v5
	v_add_u32_e32 v21, 0xe38, v5
	v_add_u32_e32 v22, 0x1040, v5
	v_add_u32_e32 v23, 0x1248, v5
	v_add_u32_e32 v24, 0x1450, v5
	v_add_u32_e32 v25, 0x1658, v5
	v_add_u32_e32 v26, 0x1860, v5
	v_add_u32_e32 v27, 0x1a68, v5
	v_add_u32_e32 v28, 0x1c70, v5
	v_add_u32_e32 v29, 0x1e78, v5
	v_add_u32_e32 v30, 0x2080, v5
	v_add_u32_e32 v31, 0x2288, v5
	v_add_u32_e32 v32, 0x2490, v5
	v_add_u32_e32 v33, 0x2698, v5
	v_add_u32_e32 v34, 0x28a0, v5
	v_add_u32_e32 v35, 0x2aa8, v5
	v_add_u32_e32 v36, 0x2cb0, v5
	v_add_u32_e32 v37, 0x2eb8, v5
	v_add_u32_e32 v38, 0x30c0, v5
	v_add_u32_e32 v39, 0x32c8, v5
	v_add_u32_e32 v40, 0x34d0, v5
	v_add_u32_e32 v41, 0x36d8, v5
	v_add_u32_e32 v42, 0x38e0, v5
	v_add_u32_e32 v43, 0x3ae8, v5
	v_add_u32_e32 v44, 0x3cf0, v5
	v_add_u32_e32 v45, 0x3ef8, v5
	s_mov_b32 s53, 0xe000
	s_movk_i32 s54, 0xb8
	s_movk_i32 s55, 0x2000
	s_mov_b32 s57, 0xa000
	s_mov_b32 s59, 0x12000
	s_mov_b32 s60, 0x16000
	s_mov_b32 s61, 0x1a000
	s_mov_b32 s62, 0x1e000
	s_mov_b32 s63, 0x22000
	s_mov_b32 s64, 0x26000
	s_mov_b32 s65, 0x2a000
	s_mov_b32 s66, 0x2e000
	s_mov_b32 s67, 0x32000
	s_mov_b32 s68, 0x36000
	s_mov_b32 s69, 0x3a000
	s_mov_b32 s70, 0x3e000
	s_mov_b32 s71, 0xb850
	v_lshlrev_b32_e32 v0, 2, v0
	v_lshlrev_b32_e32 v2, 1, v2
	v_add_u32_e32 v46, 0x400, v6
	s_mov_b32 s72, s56
	s_branch .LBB0_19

.LBB0_828:
	s_add_i32 s15, s0, 0xc00
	s_ashr_i32 s14, s15, 31
	s_lshr_b32 s14, s14, 23
	s_add_i32 s16, s15, s14
	s_ashr_i32 s14, s16, 9
	s_and_b32 s16, s16, 0xfe00
	s_sub_i32 s44, s15, s16
	s_ashr_i32 s15, s14, 31
	s_sext_i32_i16 s45, s44
	s_lshl_b64 s[16:17], s[14:15], 23
	s_bfe_u32 s14, s45, 0x5001a
	s_add_i32 s14, s44, s14
	s_sext_i32_i16 s15, s14
	s_and_b32 s14, s14, 0xffe0
	s_ashr_i32 s46, s15, 5
	s_sub_i32 s14, s44, s14
	s_waitcnt lgkmcnt(0)
	s_add_u32 s47, s10, s16
	s_addc_u32 s15, s11, s17
	s_add_u32 s45, s12, s16
	s_addc_u32 s44, s13, s17
	s_lshl_b32 s16, s46, 6
	s_lshl_b32 s17, s46, 7
	s_sext_i32_i16 s14, s14
	s_and_b32 s46, s17, 0xffffff00
	s_and_b32 s48, s16, 64
	s_ashr_i32 s17, s16, 31
	s_lshl_b32 s14, s14, 6
	s_or_b32 s46, s48, s46
	s_lshl_b64 s[16:17], s[16:17], 2
	v_add_u32_e32 v4, s14, v6
	s_add_u32 s16, s47, s16
	v_ashrrev_i32_e32 v5, 31, v4
	s_addc_u32 s17, s15, s17
	v_lshlrev_b64 v[4:5], 12, v[4:5]
	v_lshl_add_u64 v[58:59], s[16:17], 0, v[0:1]
	v_lshl_add_u64 v[4:5], v[58:59], 0, v[4:5]
	v_add_co_u32_e32 v58, vcc, s1, v4
	s_ashr_i32 s15, s14, 31
	s_nop 0
	v_addc_co_u32_e32 v59, vcc, 0, v5, vcc
	v_add_co_u32_e32 v60, vcc, s4, v4
	v_add_u32_e32 v42, s46, v7
	s_nop 0
	v_addc_co_u32_e32 v61, vcc, 0, v5, vcc
	v_add_co_u32_e32 v62, vcc, s5, v4
	s_lshl_b64 s[14:15], s[14:15], 1
	s_nop 0
	v_addc_co_u32_e32 v63, vcc, 0, v5, vcc
	v_add_co_u32_e32 v64, vcc, s6, v4
	v_add_u32_e32 v44, 8, v42
	s_nop 0
	v_addc_co_u32_e32 v65, vcc, 0, v5, vcc
	v_add_co_u32_e32 v66, vcc, s7, v4
	v_add_u32_e32 v46, 16, v42
	s_nop 0
	v_addc_co_u32_e32 v67, vcc, 0, v5, vcc
	v_add_co_u32_e32 v68, vcc, s8, v4
	v_add_u32_e32 v48, 24, v42
	s_nop 0
	v_addc_co_u32_e32 v69, vcc, 0, v5, vcc
	v_add_co_u32_e32 v70, vcc, s9, v4
	v_add_u32_e32 v50, 32, v42
	s_nop 0
	v_addc_co_u32_e32 v71, vcc, 0, v5, vcc
	v_add_co_u32_e32 v72, vcc, s18, v4
	v_add_u32_e32 v52, 40, v42
	s_nop 0
	v_addc_co_u32_e32 v73, vcc, 0, v5, vcc
	v_add_co_u32_e32 v74, vcc, s19, v4
	v_add_u32_e32 v54, 48, v42
	s_nop 0
	v_addc_co_u32_e32 v75, vcc, 0, v5, vcc
	v_add_co_u32_e32 v76, vcc, s20, v4
	v_add_u32_e32 v56, 56, v42
	s_nop 0
	v_addc_co_u32_e32 v77, vcc, 0, v5, vcc
	v_add_co_u32_e32 v78, vcc, s21, v4
	s_add_u32 s14, s45, s14
	s_nop 0
	v_addc_co_u32_e32 v79, vcc, 0, v5, vcc
	v_add_co_u32_e32 v80, vcc, s22, v4
	v_ashrrev_i32_e32 v43, 31, v42
	s_nop 0
	v_addc_co_u32_e32 v81, vcc, 0, v5, vcc
	v_add_co_u32_e32 v82, vcc, s23, v4
	v_ashrrev_i32_e32 v45, 31, v44
	s_nop 0
	v_addc_co_u32_e32 v83, vcc, 0, v5, vcc
	v_add_co_u32_e32 v84, vcc, s24, v4
	v_ashrrev_i32_e32 v47, 31, v46
	s_nop 0
	v_addc_co_u32_e32 v85, vcc, 0, v5, vcc
	v_add_co_u32_e32 v86, vcc, s25, v4
	v_ashrrev_i32_e32 v49, 31, v48
	s_nop 0
	v_addc_co_u32_e32 v87, vcc, 0, v5, vcc
	v_add_co_u32_e32 v88, vcc, s26, v4
	v_ashrrev_i32_e32 v51, 31, v50
	s_nop 0
	v_addc_co_u32_e32 v89, vcc, 0, v5, vcc
	v_add_co_u32_e32 v90, vcc, s27, v4
	v_ashrrev_i32_e32 v53, 31, v52
	s_nop 0
	v_addc_co_u32_e32 v91, vcc, 0, v5, vcc
	v_add_co_u32_e32 v92, vcc, s28, v4
	v_ashrrev_i32_e32 v55, 31, v54
	s_nop 0
	v_addc_co_u32_e32 v93, vcc, 0, v5, vcc
	v_add_co_u32_e32 v94, vcc, s29, v4
	v_ashrrev_i32_e32 v57, 31, v56
	s_nop 0
	v_addc_co_u32_e32 v95, vcc, 0, v5, vcc
	v_add_co_u32_e32 v96, vcc, s30, v4
	s_addc_u32 s15, s44, s15
	s_nop 0
	v_addc_co_u32_e32 v97, vcc, 0, v5, vcc
	v_add_co_u32_e32 v98, vcc, s31, v4
	v_lshlrev_b64 v[42:43], 12, v[42:43]
	s_nop 0
	v_addc_co_u32_e32 v99, vcc, 0, v5, vcc
	v_add_co_u32_e32 v100, vcc, s34, v4
	v_lshlrev_b64 v[44:45], 12, v[44:45]
	s_nop 0
	v_addc_co_u32_e32 v101, vcc, 0, v5, vcc
	v_add_co_u32_e32 v102, vcc, s35, v4
	v_lshlrev_b64 v[46:47], 12, v[46:47]
	s_nop 0
	v_addc_co_u32_e32 v103, vcc, 0, v5, vcc
	v_add_co_u32_e32 v104, vcc, s36, v4
	v_lshlrev_b64 v[48:49], 12, v[48:49]
	s_nop 0
	v_addc_co_u32_e32 v105, vcc, 0, v5, vcc
	v_add_co_u32_e32 v106, vcc, s37, v4
	v_lshlrev_b64 v[50:51], 12, v[50:51]
	s_nop 0
	v_addc_co_u32_e32 v107, vcc, 0, v5, vcc
	v_add_co_u32_e32 v108, vcc, s38, v4
	v_lshlrev_b64 v[52:53], 12, v[52:53]
	s_nop 0
	v_addc_co_u32_e32 v109, vcc, 0, v5, vcc
	v_add_co_u32_e32 v110, vcc, s39, v4
	v_lshlrev_b64 v[54:55], 12, v[54:55]
	s_nop 0
	v_addc_co_u32_e32 v111, vcc, 0, v5, vcc
	v_add_co_u32_e32 v112, vcc, s40, v4
	v_lshlrev_b64 v[56:57], 12, v[56:57]
	s_nop 0
	v_addc_co_u32_e32 v113, vcc, 0, v5, vcc
	v_add_co_u32_e32 v114, vcc, s41, v4
	v_lshl_add_u64 v[120:121], s[14:15], 0, v[2:3]
	s_nop 0
	v_addc_co_u32_e32 v115, vcc, 0, v5, vcc
	v_add_co_u32_e32 v116, vcc, s42, v4
	v_lshl_add_u64 v[122:123], v[120:121], 0, v[42:43]
	s_nop 0
	v_addc_co_u32_e32 v117, vcc, 0, v5, vcc
	v_add_co_u32_e32 v118, vcc, s43, v4
	v_lshl_add_u64 v[124:125], v[120:121], 0, v[44:45]
	s_nop 0
	v_addc_co_u32_e32 v119, vcc, 0, v5, vcc
	global_load_dwordx2 v[4:5], v[4:5], off nt
	s_nop 0
	global_load_dwordx2 v[58:59], v[58:59], off nt
	s_nop 0
	global_load_dwordx2 v[60:61], v[60:61], off nt
	s_nop 0
	global_load_dwordx2 v[62:63], v[62:63], off nt
	s_nop 0
	global_load_dwordx2 v[64:65], v[64:65], off nt
	s_nop 0
	global_load_dwordx2 v[66:67], v[66:67], off nt
	s_nop 0
	global_load_dwordx2 v[68:69], v[68:69], off nt
	s_nop 0
	global_load_dwordx2 v[70:71], v[70:71], off nt
	s_nop 0
	global_load_dwordx2 v[72:73], v[72:73], off nt
	s_nop 0
	global_load_dwordx2 v[74:75], v[74:75], off nt
	s_nop 0
	global_load_dwordx2 v[76:77], v[76:77], off nt
	s_nop 0
	global_load_dwordx2 v[78:79], v[78:79], off nt
	s_nop 0
	global_load_dwordx2 v[80:81], v[80:81], off nt
	s_nop 0
	global_load_dwordx2 v[82:83], v[82:83], off nt
	s_nop 0
	global_load_dwordx2 v[84:85], v[84:85], off nt
	s_nop 0
	global_load_dwordx2 v[86:87], v[86:87], off nt
	s_nop 0
	global_load_dwordx2 v[88:89], v[88:89], off nt
	s_nop 0
	global_load_dwordx2 v[90:91], v[90:91], off nt
	s_nop 0
	global_load_dwordx2 v[92:93], v[92:93], off nt
	s_nop 0
	global_load_dwordx2 v[94:95], v[94:95], off nt
	s_nop 0
	global_load_dwordx2 v[96:97], v[96:97], off nt
	s_nop 0
	global_load_dwordx2 v[98:99], v[98:99], off nt
	s_nop 0
	global_load_dwordx2 v[100:101], v[100:101], off nt
	s_nop 0
	global_load_dwordx2 v[102:103], v[102:103], off nt
	s_nop 0
	global_load_dwordx2 v[104:105], v[104:105], off nt
	s_nop 0
	global_load_dwordx2 v[106:107], v[106:107], off nt
	s_nop 0
	global_load_dwordx2 v[108:109], v[108:109], off nt
	s_nop 0
	global_load_dwordx2 v[110:111], v[110:111], off nt
	s_nop 0
	global_load_dwordx2 v[112:113], v[112:113], off nt
	s_nop 0
	global_load_dwordx2 v[114:115], v[114:115], off nt
	s_nop 0
	global_load_dwordx2 v[116:117], v[116:117], off nt
	s_nop 0
	global_load_dwordx2 v[118:119], v[118:119], off nt
	s_waitcnt vmcnt(0)
	ds_write2_b32 v9, v4, v5 offset1:1
	ds_write2_b32 v9, v58, v59 offset0:130 offset1:131
	ds_write2_b32 v10, v60, v61 offset1:1
	ds_write2_b32 v11, v62, v63 offset1:1
	ds_write2_b32 v12, v64, v65 offset1:1
	ds_write2_b32 v13, v66, v67 offset1:1
	ds_write2_b32 v14, v68, v69 offset1:1
	ds_write2_b32 v15, v70, v71 offset1:1
	ds_write2_b32 v16, v72, v73 offset1:1
	ds_write2_b32 v17, v74, v75 offset1:1
	ds_write2_b32 v18, v76, v77 offset1:1
	ds_write2_b32 v19, v78, v79 offset1:1
	ds_write2_b32 v20, v80, v81 offset1:1
	ds_write2_b32 v21, v82, v83 offset1:1
	ds_write2_b32 v22, v84, v85 offset1:1
	ds_write2_b32 v23, v86, v87 offset1:1
	ds_write2_b32 v24, v88, v89 offset1:1
	ds_write2_b32 v25, v90, v91 offset1:1
	ds_write2_b32 v26, v92, v93 offset1:1
	ds_write2_b32 v27, v94, v95 offset1:1
	ds_write2_b32 v28, v96, v97 offset1:1
	ds_write2_b32 v29, v98, v99 offset1:1
	ds_write2_b32 v30, v100, v101 offset1:1
	ds_write2_b32 v31, v102, v103 offset1:1
	ds_write2_b32 v32, v104, v105 offset1:1
	ds_write2_b32 v33, v106, v107 offset1:1
	ds_write2_b32 v34, v108, v109 offset1:1
	ds_write2_b32 v35, v110, v111 offset1:1
	ds_write2_b32 v36, v112, v113 offset1:1
	ds_write2_b32 v37, v114, v115 offset1:1
	ds_write2_b32 v38, v116, v117 offset1:1
	ds_write2_b32 v39, v118, v119 offset1:1
	s_waitcnt lgkmcnt(0)
	v_lshl_add_u64 v[126:127], v[120:121], 0, v[46:47]
	v_lshl_add_u64 v[128:129], v[120:121], 0, v[48:49]
	v_lshl_add_u64 v[130:131], v[120:121], 0, v[50:51]
	v_lshl_add_u64 v[132:133], v[120:121], 0, v[52:53]
	v_lshl_add_u64 v[134:135], v[120:121], 0, v[54:55]
	v_lshl_add_u64 v[120:121], v[120:121], 0, v[56:57]
	ds_read2_b32 v[4:5], v8 offset0:65 offset1:73
	ds_read2_b32 v[46:47], v8 offset1:8
	ds_read2_b32 v[48:49], v8 offset0:130 offset1:138
	ds_read2_b32 v[50:51], v8 offset0:195 offset1:203
	ds_read2_b32 v[52:53], v40 offset0:4 offset1:12
	ds_read2_b32 v[54:55], v40 offset0:69 offset1:77
	ds_read2_b32 v[56:57], v40 offset0:134 offset1:142
	ds_read2_b32 v[58:59], v40 offset0:199 offset1:207
	ds_read2_b32 v[60:61], v8 offset0:81 offset1:89
	ds_read2_b32 v[62:63], v8 offset0:16 offset1:24
	ds_read2_b32 v[64:65], v8 offset0:146 offset1:154
	ds_read2_b32 v[66:67], v8 offset0:211 offset1:219
	ds_read2_b32 v[68:69], v40 offset0:20 offset1:28
	ds_read2_b32 v[70:71], v40 offset0:85 offset1:93
	ds_read2_b32 v[72:73], v40 offset0:150 offset1:158
	ds_read2_b32 v[74:75], v40 offset0:215 offset1:223
	ds_read2_b32 v[76:77], v8 offset0:32 offset1:40
	ds_read2_b32 v[78:79], v8 offset0:97 offset1:105
	ds_read2_b32 v[80:81], v8 offset0:162 offset1:170
	ds_read2_b32 v[82:83], v8 offset0:227 offset1:235
	ds_read2_b32 v[84:85], v40 offset0:36 offset1:44
	ds_read2_b32 v[86:87], v40 offset0:101 offset1:109
	ds_read2_b32 v[88:89], v40 offset0:166 offset1:174
	ds_read2_b32 v[90:91], v40 offset0:231 offset1:239
	ds_read2_b32 v[92:93], v8 offset0:48 offset1:56
	ds_read2_b32 v[94:95], v8 offset0:113 offset1:121
	ds_read2_b32 v[96:97], v8 offset0:178 offset1:186
	ds_read2_b32 v[98:99], v8 offset0:243 offset1:251
	ds_read2_b32 v[100:101], v40 offset0:52 offset1:60
	ds_read2_b32 v[102:103], v40 offset0:117 offset1:125
	ds_read2_b32 v[104:105], v40 offset0:182 offset1:190
	ds_read2_b32 v[106:107], v40 offset0:247 offset1:255
	s_waitcnt lgkmcnt(14)
	v_cvt_pk_bf16_f32 v42, v46, v4
	v_cvt_pk_bf16_f32 v43, v48, v50
	v_cvt_pk_bf16_f32 v44, v52, v54
	v_cvt_pk_bf16_f32 v45, v56, v58
	v_cvt_pk_bf16_f32 v46, v47, v5
	v_cvt_pk_bf16_f32 v47, v49, v51
	v_cvt_pk_bf16_f32 v48, v53, v55
	v_cvt_pk_bf16_f32 v49, v57, v59
	v_cvt_pk_bf16_f32 v50, v62, v60
	v_cvt_pk_bf16_f32 v51, v64, v66
	v_cvt_pk_bf16_f32 v52, v68, v70
	v_cvt_pk_bf16_f32 v53, v72, v74
	v_cvt_pk_bf16_f32 v54, v63, v61
	v_cvt_pk_bf16_f32 v55, v65, v67
	v_cvt_pk_bf16_f32 v56, v69, v71
	v_cvt_pk_bf16_f32 v57, v73, v75
	v_cvt_pk_bf16_f32 v58, v76, v78
	s_waitcnt lgkmcnt(12)
	v_cvt_pk_bf16_f32 v59, v80, v82
	s_waitcnt lgkmcnt(10)
	v_cvt_pk_bf16_f32 v60, v84, v86
	s_waitcnt lgkmcnt(8)
	v_cvt_pk_bf16_f32 v61, v88, v90
	v_cvt_pk_bf16_f32 v62, v77, v79
	v_cvt_pk_bf16_f32 v63, v81, v83
	v_cvt_pk_bf16_f32 v64, v85, v87
	v_cvt_pk_bf16_f32 v65, v89, v91
	s_waitcnt lgkmcnt(6)
	v_cvt_pk_bf16_f32 v66, v92, v94
	s_waitcnt lgkmcnt(4)
	v_cvt_pk_bf16_f32 v67, v96, v98
	s_waitcnt lgkmcnt(2)
	v_cvt_pk_bf16_f32 v68, v100, v102
	s_waitcnt lgkmcnt(0)
	v_cvt_pk_bf16_f32 v69, v104, v106
	v_cvt_pk_bf16_f32 v70, v93, v95
	v_cvt_pk_bf16_f32 v71, v97, v99
	v_cvt_pk_bf16_f32 v72, v101, v103
	v_cvt_pk_bf16_f32 v73, v105, v107
	global_store_dwordx4 v[122:123], v[42:45], off nt
	global_store_dwordx4 v[124:125], v[46:49], off nt
	global_store_dwordx4 v[126:127], v[50:53], off nt
	global_store_dwordx4 v[128:129], v[54:57], off nt
	global_store_dwordx4 v[130:131], v[58:61], off nt
	global_store_dwordx4 v[132:133], v[62:65], off nt
	global_store_dwordx4 v[134:135], v[66:69], off nt
	global_store_dwordx4 v[120:121], v[70:73], off nt
	s_waitcnt lgkmcnt(0)
	s_addk_i32 s0, 0x400
	s_cmpk_gt_i32 s0, 0xfff
	s_cbranch_scc0 .LBB0_828

.LBB0_2219:
	s_add_i32 s11, s0, 0xc00
	s_ashr_i32 s10, s11, 31
	s_lshr_b32 s10, s10, 23
	s_add_i32 s12, s11, s10
	s_ashr_i32 s10, s12, 9
	s_and_b32 s12, s12, 0xfe00
	s_sub_i32 s12, s11, s12
	s_sext_i32_i16 s13, s12
	s_bfe_u32 s13, s13, 0x5001a
	s_add_i32 s13, s12, s13
	s_ashr_i32 s11, s10, 31
	s_sext_i32_i16 s44, s13
	s_and_b32 s13, s13, 0xffe0
	s_lshl_b64 s[10:11], s[10:11], 23
	s_ashr_i32 s46, s44, 5
	s_sub_i32 s12, s12, s13
	s_add_u32 s10, s10, 0x8000000
	s_sext_i32_i16 s13, s12
	s_addc_u32 s12, s11, 0
	s_waitcnt lgkmcnt(0)
	s_add_u32 s47, s6, s10
	s_addc_u32 s11, s7, s12
	s_add_u32 s45, s8, s10
	s_addc_u32 s44, s9, s12
	s_lshl_b32 s12, s46, 6
	s_lshl_b32 s10, s13, 6
	s_lshl_b32 s13, s46, 7
	s_and_b32 s46, s13, 0xffffff00
	s_and_b32 s48, s12, 64
	s_ashr_i32 s13, s12, 31
	s_or_b32 s46, s48, s46
	s_lshl_b64 s[12:13], s[12:13], 2
	v_add_u32_e32 v4, s10, v74
	s_add_u32 s12, s47, s12
	v_ashrrev_i32_e32 v5, 31, v4
	s_addc_u32 s13, s11, s13
	v_lshlrev_b64 v[4:5], 12, v[4:5]
	v_lshl_add_u64 v[56:57], s[12:13], 0, v[0:1]
	v_lshl_add_u64 v[4:5], v[56:57], 0, v[4:5]
	v_add_co_u32_e32 v56, vcc, s1, v4
	s_ashr_i32 s11, s10, 31
	s_nop 0
	v_addc_co_u32_e32 v57, vcc, 0, v5, vcc
	v_add_co_u32_e32 v58, vcc, s4, v4
	v_add_u32_e32 v40, s46, v75
	s_nop 0
	v_addc_co_u32_e32 v59, vcc, 0, v5, vcc
	v_add_co_u32_e32 v60, vcc, s5, v4
	s_lshl_b64 s[10:11], s[10:11], 1
	s_nop 0
	v_addc_co_u32_e32 v61, vcc, 0, v5, vcc
	v_add_co_u32_e32 v62, vcc, s14, v4
	v_add_u32_e32 v42, 8, v40
	s_nop 0
	v_addc_co_u32_e32 v63, vcc, 0, v5, vcc
	v_add_co_u32_e32 v64, vcc, s15, v4
	v_add_u32_e32 v44, 16, v40
	s_nop 0
	v_addc_co_u32_e32 v65, vcc, 0, v5, vcc
	v_add_co_u32_e32 v66, vcc, s16, v4
	v_add_u32_e32 v46, 24, v40
	s_nop 0
	v_addc_co_u32_e32 v67, vcc, 0, v5, vcc
	v_add_co_u32_e32 v68, vcc, s17, v4
	v_add_u32_e32 v48, 32, v40
	s_nop 0
	v_addc_co_u32_e32 v69, vcc, 0, v5, vcc
	v_add_co_u32_e32 v70, vcc, s18, v4
	v_add_u32_e32 v50, 40, v40
	s_nop 0
	v_addc_co_u32_e32 v71, vcc, 0, v5, vcc
	v_add_co_u32_e32 v72, vcc, s19, v4
	v_add_u32_e32 v52, 48, v40
	s_nop 0
	v_addc_co_u32_e32 v73, vcc, 0, v5, vcc
	v_add_co_u32_e32 v76, vcc, s20, v4
	v_add_u32_e32 v54, 56, v40
	s_nop 0
	v_addc_co_u32_e32 v77, vcc, 0, v5, vcc
	v_add_co_u32_e32 v78, vcc, s21, v4
	s_add_u32 s10, s45, s10
	s_nop 0
	v_addc_co_u32_e32 v79, vcc, 0, v5, vcc
	v_add_co_u32_e32 v80, vcc, s22, v4
	v_ashrrev_i32_e32 v41, 31, v40
	s_nop 0
	v_addc_co_u32_e32 v81, vcc, 0, v5, vcc
	v_add_co_u32_e32 v82, vcc, s23, v4
	v_ashrrev_i32_e32 v43, 31, v42
	s_nop 0
	v_addc_co_u32_e32 v83, vcc, 0, v5, vcc
	v_add_co_u32_e32 v84, vcc, s24, v4
	v_ashrrev_i32_e32 v45, 31, v44
	s_nop 0
	v_addc_co_u32_e32 v85, vcc, 0, v5, vcc
	v_add_co_u32_e32 v86, vcc, s25, v4
	v_ashrrev_i32_e32 v47, 31, v46
	s_nop 0
	v_addc_co_u32_e32 v87, vcc, 0, v5, vcc
	v_add_co_u32_e32 v88, vcc, s26, v4
	v_ashrrev_i32_e32 v49, 31, v48
	s_nop 0
	v_addc_co_u32_e32 v89, vcc, 0, v5, vcc
	v_add_co_u32_e32 v90, vcc, s27, v4
	v_ashrrev_i32_e32 v51, 31, v50
	s_nop 0
	v_addc_co_u32_e32 v91, vcc, 0, v5, vcc
	v_add_co_u32_e32 v92, vcc, s28, v4
	v_ashrrev_i32_e32 v53, 31, v52
	s_nop 0
	v_addc_co_u32_e32 v93, vcc, 0, v5, vcc
	v_add_co_u32_e32 v94, vcc, s29, v4
	v_ashrrev_i32_e32 v55, 31, v54
	s_nop 0
	v_addc_co_u32_e32 v95, vcc, 0, v5, vcc
	v_add_co_u32_e32 v96, vcc, s30, v4
	s_addc_u32 s11, s44, s11
	s_nop 0
	v_addc_co_u32_e32 v97, vcc, 0, v5, vcc
	v_add_co_u32_e32 v98, vcc, s31, v4
	v_lshlrev_b64 v[40:41], 12, v[40:41]
	s_nop 0
	v_addc_co_u32_e32 v99, vcc, 0, v5, vcc
	v_add_co_u32_e32 v100, vcc, s34, v4
	v_lshlrev_b64 v[42:43], 12, v[42:43]
	s_nop 0
	v_addc_co_u32_e32 v101, vcc, 0, v5, vcc
	v_add_co_u32_e32 v102, vcc, s35, v4
	v_lshlrev_b64 v[44:45], 12, v[44:45]
	s_nop 0
	v_addc_co_u32_e32 v103, vcc, 0, v5, vcc
	v_add_co_u32_e32 v104, vcc, s36, v4
	v_lshlrev_b64 v[46:47], 12, v[46:47]
	s_nop 0
	v_addc_co_u32_e32 v105, vcc, 0, v5, vcc
	v_add_co_u32_e32 v106, vcc, s37, v4
	v_lshlrev_b64 v[48:49], 12, v[48:49]
	s_nop 0
	v_addc_co_u32_e32 v107, vcc, 0, v5, vcc
	v_add_co_u32_e32 v108, vcc, s38, v4
	v_lshlrev_b64 v[50:51], 12, v[50:51]
	s_nop 0
	v_addc_co_u32_e32 v109, vcc, 0, v5, vcc
	v_add_co_u32_e32 v110, vcc, s39, v4
	v_lshlrev_b64 v[52:53], 12, v[52:53]
	s_nop 0
	v_addc_co_u32_e32 v111, vcc, 0, v5, vcc
	v_add_co_u32_e32 v112, vcc, s40, v4
	v_lshlrev_b64 v[54:55], 12, v[54:55]
	s_nop 0
	v_addc_co_u32_e32 v113, vcc, 0, v5, vcc
	v_add_co_u32_e32 v114, vcc, s41, v4
	v_lshl_add_u64 v[120:121], s[10:11], 0, v[2:3]
	s_nop 0
	v_addc_co_u32_e32 v115, vcc, 0, v5, vcc
	v_add_co_u32_e32 v116, vcc, s42, v4
	v_lshl_add_u64 v[122:123], v[120:121], 0, v[40:41]
	s_nop 0
	v_addc_co_u32_e32 v117, vcc, 0, v5, vcc
	v_add_co_u32_e32 v118, vcc, s43, v4
	v_lshl_add_u64 v[124:125], v[120:121], 0, v[42:43]
	s_nop 0
	v_addc_co_u32_e32 v119, vcc, 0, v5, vcc
	global_load_dwordx2 v[4:5], v[4:5], off nt
	s_nop 0
	global_load_dwordx2 v[56:57], v[56:57], off nt
	s_nop 0
	global_load_dwordx2 v[58:59], v[58:59], off nt
	s_nop 0
	global_load_dwordx2 v[60:61], v[60:61], off nt
	s_nop 0
	global_load_dwordx2 v[62:63], v[62:63], off nt
	s_nop 0
	global_load_dwordx2 v[64:65], v[64:65], off nt
	s_nop 0
	global_load_dwordx2 v[66:67], v[66:67], off nt
	s_nop 0
	global_load_dwordx2 v[68:69], v[68:69], off nt
	s_nop 0
	global_load_dwordx2 v[70:71], v[70:71], off nt
	s_nop 0
	global_load_dwordx2 v[72:73], v[72:73], off nt
	s_nop 0
	global_load_dwordx2 v[76:77], v[76:77], off nt
	s_nop 0
	global_load_dwordx2 v[78:79], v[78:79], off nt
	s_nop 0
	global_load_dwordx2 v[80:81], v[80:81], off nt
	s_nop 0
	global_load_dwordx2 v[82:83], v[82:83], off nt
	s_nop 0
	global_load_dwordx2 v[84:85], v[84:85], off nt
	s_nop 0
	global_load_dwordx2 v[86:87], v[86:87], off nt
	s_nop 0
	global_load_dwordx2 v[88:89], v[88:89], off nt
	s_nop 0
	global_load_dwordx2 v[90:91], v[90:91], off nt
	s_nop 0
	global_load_dwordx2 v[92:93], v[92:93], off nt
	s_nop 0
	global_load_dwordx2 v[94:95], v[94:95], off nt
	s_nop 0
	global_load_dwordx2 v[96:97], v[96:97], off nt
	s_nop 0
	global_load_dwordx2 v[98:99], v[98:99], off nt
	s_nop 0
	global_load_dwordx2 v[100:101], v[100:101], off nt
	s_nop 0
	global_load_dwordx2 v[102:103], v[102:103], off nt
	s_nop 0
	global_load_dwordx2 v[104:105], v[104:105], off nt
	s_nop 0
	global_load_dwordx2 v[106:107], v[106:107], off nt
	s_nop 0
	global_load_dwordx2 v[108:109], v[108:109], off nt
	s_nop 0
	global_load_dwordx2 v[110:111], v[110:111], off nt
	s_nop 0
	global_load_dwordx2 v[112:113], v[112:113], off nt
	s_nop 0
	global_load_dwordx2 v[114:115], v[114:115], off nt
	s_nop 0
	global_load_dwordx2 v[116:117], v[116:117], off nt
	s_nop 0
	global_load_dwordx2 v[118:119], v[118:119], off nt
	s_waitcnt vmcnt(0)
	ds_write2_b32 v7, v4, v5 offset1:1
	ds_write2_b32 v7, v56, v57 offset0:130 offset1:131
	ds_write2_b32 v8, v58, v59 offset1:1
	ds_write2_b32 v9, v60, v61 offset1:1
	ds_write2_b32 v10, v62, v63 offset1:1
	ds_write2_b32 v11, v64, v65 offset1:1
	ds_write2_b32 v12, v66, v67 offset1:1
	ds_write2_b32 v13, v68, v69 offset1:1
	ds_write2_b32 v14, v70, v71 offset1:1
	ds_write2_b32 v15, v72, v73 offset1:1
	ds_write2_b32 v16, v76, v77 offset1:1
	ds_write2_b32 v17, v78, v79 offset1:1
	ds_write2_b32 v18, v80, v81 offset1:1
	ds_write2_b32 v19, v82, v83 offset1:1
	ds_write2_b32 v20, v84, v85 offset1:1
	ds_write2_b32 v21, v86, v87 offset1:1
	ds_write2_b32 v22, v88, v89 offset1:1
	ds_write2_b32 v23, v90, v91 offset1:1
	ds_write2_b32 v24, v92, v93 offset1:1
	ds_write2_b32 v25, v94, v95 offset1:1
	ds_write2_b32 v26, v96, v97 offset1:1
	ds_write2_b32 v27, v98, v99 offset1:1
	ds_write2_b32 v28, v100, v101 offset1:1
	ds_write2_b32 v29, v102, v103 offset1:1
	ds_write2_b32 v30, v104, v105 offset1:1
	ds_write2_b32 v31, v106, v107 offset1:1
	ds_write2_b32 v32, v108, v109 offset1:1
	ds_write2_b32 v33, v110, v111 offset1:1
	ds_write2_b32 v34, v112, v113 offset1:1
	ds_write2_b32 v35, v114, v115 offset1:1
	ds_write2_b32 v36, v116, v117 offset1:1
	ds_write2_b32 v37, v118, v119 offset1:1
	s_waitcnt lgkmcnt(0)
	v_lshl_add_u64 v[126:127], v[120:121], 0, v[44:45]
	v_lshl_add_u64 v[128:129], v[120:121], 0, v[46:47]
	v_lshl_add_u64 v[130:131], v[120:121], 0, v[48:49]
	v_lshl_add_u64 v[132:133], v[120:121], 0, v[50:51]
	v_lshl_add_u64 v[134:135], v[120:121], 0, v[52:53]
	v_lshl_add_u64 v[120:121], v[120:121], 0, v[54:55]
	ds_read2_b32 v[4:5], v6 offset0:65 offset1:73
	ds_read2_b32 v[44:45], v6 offset1:8
	ds_read2_b32 v[46:47], v6 offset0:130 offset1:138
	ds_read2_b32 v[48:49], v6 offset0:195 offset1:203
	ds_read2_b32 v[50:51], v38 offset0:4 offset1:12
	ds_read2_b32 v[52:53], v38 offset0:69 offset1:77
	ds_read2_b32 v[54:55], v38 offset0:134 offset1:142
	ds_read2_b32 v[56:57], v38 offset0:199 offset1:207
	ds_read2_b32 v[58:59], v6 offset0:81 offset1:89
	ds_read2_b32 v[60:61], v6 offset0:16 offset1:24
	ds_read2_b32 v[62:63], v6 offset0:146 offset1:154
	ds_read2_b32 v[64:65], v6 offset0:211 offset1:219
	ds_read2_b32 v[66:67], v38 offset0:20 offset1:28
	ds_read2_b32 v[68:69], v38 offset0:85 offset1:93
	ds_read2_b32 v[70:71], v38 offset0:150 offset1:158
	ds_read2_b32 v[72:73], v38 offset0:215 offset1:223
	ds_read2_b32 v[76:77], v6 offset0:32 offset1:40
	ds_read2_b32 v[78:79], v6 offset0:97 offset1:105
	ds_read2_b32 v[80:81], v6 offset0:162 offset1:170
	ds_read2_b32 v[82:83], v6 offset0:227 offset1:235
	ds_read2_b32 v[84:85], v38 offset0:36 offset1:44
	ds_read2_b32 v[86:87], v38 offset0:101 offset1:109
	ds_read2_b32 v[88:89], v38 offset0:166 offset1:174
	ds_read2_b32 v[90:91], v38 offset0:231 offset1:239
	ds_read2_b32 v[92:93], v6 offset0:48 offset1:56
	ds_read2_b32 v[94:95], v6 offset0:113 offset1:121
	ds_read2_b32 v[96:97], v6 offset0:178 offset1:186
	ds_read2_b32 v[98:99], v6 offset0:243 offset1:251
	ds_read2_b32 v[100:101], v38 offset0:52 offset1:60
	ds_read2_b32 v[102:103], v38 offset0:117 offset1:125
	ds_read2_b32 v[104:105], v38 offset0:182 offset1:190
	ds_read2_b32 v[106:107], v38 offset0:247 offset1:255
	s_waitcnt lgkmcnt(14)
	v_cvt_pk_bf16_f32 v40, v44, v4
	v_cvt_pk_bf16_f32 v41, v46, v48
	v_cvt_pk_bf16_f32 v42, v50, v52
	v_cvt_pk_bf16_f32 v43, v54, v56
	v_cvt_pk_bf16_f32 v44, v45, v5
	v_cvt_pk_bf16_f32 v45, v47, v49
	v_cvt_pk_bf16_f32 v46, v51, v53
	v_cvt_pk_bf16_f32 v47, v55, v57
	v_cvt_pk_bf16_f32 v48, v60, v58
	v_cvt_pk_bf16_f32 v49, v62, v64
	v_cvt_pk_bf16_f32 v50, v66, v68
	v_cvt_pk_bf16_f32 v51, v70, v72
	v_cvt_pk_bf16_f32 v52, v61, v59
	v_cvt_pk_bf16_f32 v53, v63, v65
	v_cvt_pk_bf16_f32 v54, v67, v69
	v_cvt_pk_bf16_f32 v55, v71, v73
	v_cvt_pk_bf16_f32 v56, v76, v78
	s_waitcnt lgkmcnt(12)
	v_cvt_pk_bf16_f32 v57, v80, v82
	s_waitcnt lgkmcnt(10)
	v_cvt_pk_bf16_f32 v58, v84, v86
	s_waitcnt lgkmcnt(8)
	v_cvt_pk_bf16_f32 v59, v88, v90
	v_cvt_pk_bf16_f32 v60, v77, v79
	v_cvt_pk_bf16_f32 v61, v81, v83
	v_cvt_pk_bf16_f32 v62, v85, v87
	v_cvt_pk_bf16_f32 v63, v89, v91
	s_waitcnt lgkmcnt(6)
	v_cvt_pk_bf16_f32 v64, v92, v94
	s_waitcnt lgkmcnt(4)
	v_cvt_pk_bf16_f32 v65, v96, v98
	s_waitcnt lgkmcnt(2)
	v_cvt_pk_bf16_f32 v66, v100, v102
	s_waitcnt lgkmcnt(0)
	v_cvt_pk_bf16_f32 v67, v104, v106
	v_cvt_pk_bf16_f32 v68, v93, v95
	v_cvt_pk_bf16_f32 v69, v97, v99
	v_cvt_pk_bf16_f32 v70, v101, v103
	v_cvt_pk_bf16_f32 v71, v105, v107
	global_store_dwordx4 v[122:123], v[40:43], off nt
	global_store_dwordx4 v[124:125], v[44:47], off nt
	global_store_dwordx4 v[126:127], v[48:51], off nt
	global_store_dwordx4 v[128:129], v[52:55], off nt
	global_store_dwordx4 v[130:131], v[56:59], off nt
	global_store_dwordx4 v[132:133], v[60:63], off nt
	global_store_dwordx4 v[134:135], v[64:67], off nt
	global_store_dwordx4 v[120:121], v[68:71], off nt
	s_waitcnt lgkmcnt(0)
	s_addk_i32 s0, 0x400
	s_cmpk_gt_i32 s0, 0xfff
	s_cbranch_scc0 .LBB0_2219
